# P2 QKV GEMM epilogue: 8 per-row scale loads hoisted into one batch, per-row vmcnt(0) drains removed
# baseline (speedup 1.0000x reference)
.LBB0_200:
	v_lshl_or_b32 v156, s54, 8, v176
	v_ashrrev_i32_e32 v157, 31, v156
	v_lshl_add_u64 v[150:151], v[156:157], 2, s[8:9]
	global_load_dwordx4 v[180:183], v[150:151], off
	global_load_dwordx4 v[184:187], v[150:151], off offset:16
	global_load_dwordx4 v[188:191], v[150:151], off offset:512
	global_load_dwordx4 v[192:195], v[150:151], off offset:528
	v_lshl_add_u32 v150, s20, 8, v1
	v_ashrrev_i32_e32 v151, 31, v150
	v_lshl_add_u64 v[154:155], v[150:151], 2, s[82:83]
	global_load_dword v196, v[154:155], off
	global_load_dword v222, v[154:155], off offset:64
	global_load_dword v224, v[154:155], off offset:128
	global_load_dword v226, v[154:155], off offset:192
	global_load_dword v228, v[154:155], off offset:512
	global_load_dword v230, v[154:155], off offset:576
	global_load_dword v232, v[154:155], off offset:640
	global_load_dword v234, v[154:155], off offset:704
	s_cmp_lt_i32 s54, 4
	v_cvt_f32_i32_e32 v199, v127
	v_cvt_f32_i32_e32 v198, v126
	v_cvt_f32_i32_e32 v201, v129
	v_cvt_f32_i32_e32 v200, v128
	v_cvt_f32_i32_e32 v203, v123
	v_cvt_f32_i32_e32 v202, v122
	v_cvt_f32_i32_e32 v205, v125
	v_cvt_f32_i32_e32 v204, v124
	v_mov_b64_e32 v[152:153], s[94:95]
	v_cvt_f32_i32_e32 v207, v119
	v_cvt_f32_i32_e32 v206, v118
	v_cvt_f32_i32_e32 v209, v121
	v_cvt_f32_i32_e32 v208, v120
	v_cvt_f32_i32_e32 v211, v115
	v_cvt_f32_i32_e32 v210, v114
	v_cvt_f32_i32_e32 v213, v117
	v_cvt_f32_i32_e32 v212, v116
	s_cselect_b64 vcc, -1, 0
	v_cndmask_b32_e32 v214, 1.0, v178, vcc
	v_mad_i64_i32 v[116:117], s[22:23], v150, s51, v[152:153]
	v_lshlrev_b64 v[114:115], 1, v[156:157]
	v_lshl_add_u64 v[218:219], v[116:117], 0, v[114:115]
	v_or_b32_e32 v216, 16, v150
	v_ashrrev_i32_e32 v217, 31, v216
	v_lshl_add_u64 v[220:221], v[216:217], 2, s[82:83]
	v_cvt_f32_i32_e32 v111, v111
	v_cvt_f32_i32_e32 v110, v110
	v_cvt_f32_i32_e32 v113, v113
	v_cvt_f32_i32_e32 v112, v112
	v_cvt_f32_i32_e32 v107, v107
	v_cvt_f32_i32_e32 v106, v106
	v_cvt_f32_i32_e32 v109, v109
	v_cvt_f32_i32_e32 v108, v108
	v_cvt_f32_i32_e32 v103, v103
	v_cvt_f32_i32_e32 v102, v102
	v_cvt_f32_i32_e32 v105, v105
	v_cvt_f32_i32_e32 v104, v104
	v_cvt_f32_i32_e32 v99, v99
	v_cvt_f32_i32_e32 v98, v98
	v_cvt_f32_i32_e32 v101, v101
	v_cvt_f32_i32_e32 v100, v100
	v_cvt_f32_i32_e32 v95, v95
	v_cvt_f32_i32_e32 v94, v94
	v_cvt_f32_i32_e32 v97, v97
	v_cvt_f32_i32_e32 v96, v96
	v_cvt_f32_i32_e32 v91, v91
	v_cvt_f32_i32_e32 v90, v90
	v_cvt_f32_i32_e32 v93, v93
	v_cvt_f32_i32_e32 v92, v92
	v_cvt_f32_i32_e32 v87, v87
	v_cvt_f32_i32_e32 v86, v86
	v_cvt_f32_i32_e32 v89, v89
	v_cvt_f32_i32_e32 v88, v88
	v_cvt_f32_i32_e32 v83, v83
	v_cvt_f32_i32_e32 v82, v82
	v_cvt_f32_i32_e32 v85, v85
	v_cvt_f32_i32_e32 v84, v84
	v_cvt_f32_i32_e32 v79, v79
	v_cvt_f32_i32_e32 v78, v78
	v_cvt_f32_i32_e32 v81, v81
	v_cvt_f32_i32_e32 v80, v80
	v_cvt_f32_i32_e32 v75, v75
	v_cvt_f32_i32_e32 v74, v74
	v_cvt_f32_i32_e32 v77, v77
	v_cvt_f32_i32_e32 v76, v76
	v_cvt_f32_i32_e32 v71, v71
	v_cvt_f32_i32_e32 v70, v70
	v_cvt_f32_i32_e32 v73, v73
	v_cvt_f32_i32_e32 v72, v72
	v_cvt_f32_i32_e32 v67, v67
	s_waitcnt vmcnt(0)
	v_pk_mul_f32 v[116:117], v[214:215], v[182:183] op_sel_hi:[0,1]
	v_pk_mul_f32 v[118:119], v[214:215], v[180:181] op_sel_hi:[0,1]
	v_pk_mul_f32 v[120:121], v[214:215], v[186:187] op_sel_hi:[0,1]
	v_pk_mul_f32 v[122:123], v[214:215], v[184:185] op_sel_hi:[0,1]
	v_pk_mul_f32 v[124:125], v[214:215], v[190:191] op_sel_hi:[0,1]
	v_pk_mul_f32 v[126:127], v[214:215], v[188:189] op_sel_hi:[0,1]
	v_pk_mul_f32 v[128:129], v[214:215], v[194:195] op_sel_hi:[0,1]
	v_pk_mul_f32 v[156:157], v[214:215], v[192:193] op_sel_hi:[0,1]
	v_pk_mul_f32 v[180:181], v[116:117], v[200:201]
	v_pk_mul_f32 v[182:183], v[118:119], v[198:199]
	v_pk_mul_f32 v[184:185], v[120:121], v[204:205]
	v_pk_mul_f32 v[186:187], v[122:123], v[202:203]
	v_pk_mul_f32 v[188:189], v[124:125], v[208:209]
	v_pk_mul_f32 v[190:191], v[126:127], v[206:207]
	v_pk_mul_f32 v[192:193], v[128:129], v[212:213]
	v_pk_mul_f32 v[194:195], v[156:157], v[210:211]
	v_pk_mul_f32 v[198:199], v[180:181], v[196:197] op_sel_hi:[1,0]
	v_pk_mul_f32 v[180:181], v[182:183], v[196:197] op_sel_hi:[1,0]
	v_pk_mul_f32 v[184:185], v[184:185], v[196:197] op_sel_hi:[1,0]
	v_pk_mul_f32 v[182:183], v[186:187], v[196:197] op_sel_hi:[1,0]
	v_pk_mul_f32 v[186:187], v[188:189], v[196:197] op_sel_hi:[1,0]
	v_pk_mul_f32 v[188:189], v[190:191], v[196:197] op_sel_hi:[1,0]
	v_pk_mul_f32 v[190:191], v[192:193], v[196:197] op_sel_hi:[1,0]
	v_pk_mul_f32 v[192:193], v[194:195], v[196:197] op_sel_hi:[1,0]
	v_cvt_pk_bf16_f32 v180, v180, v181
	v_cvt_pk_bf16_f32 v181, v198, v199
	v_cvt_pk_bf16_f32 v182, v182, v183
	v_cvt_pk_bf16_f32 v183, v184, v185
	v_cvt_pk_bf16_f32 v184, v188, v189
	v_cvt_pk_bf16_f32 v185, v186, v187
	v_cvt_pk_bf16_f32 v186, v192, v193
	v_cvt_pk_bf16_f32 v187, v190, v191
	global_store_dwordx4 v[218:219], v[180:183], off
	global_store_dwordx4 v[218:219], v[184:187], off offset:256
	s_nop 0
	v_pk_mul_f32 v[112:113], v[116:117], v[112:113]
	v_pk_mul_f32 v[110:111], v[118:119], v[110:111]
	v_pk_mul_f32 v[108:109], v[120:121], v[108:109]
	v_pk_mul_f32 v[106:107], v[122:123], v[106:107]
	v_or_b32_e32 v182, 32, v150
	v_mad_i64_i32 v[184:185], s[22:23], v216, s51, v[152:153]
	v_pk_mul_f32 v[104:105], v[124:125], v[104:105]
	v_pk_mul_f32 v[102:103], v[126:127], v[102:103]
	v_pk_mul_f32 v[100:101], v[128:129], v[100:101]
	v_pk_mul_f32 v[98:99], v[156:157], v[98:99]
	v_ashrrev_i32_e32 v183, 31, v182
	v_lshl_add_u64 v[184:185], v[184:185], 0, v[114:115]
	v_lshl_add_u64 v[186:187], v[182:183], 2, s[82:83]
	v_pk_mul_f32 v[96:97], v[116:117], v[96:97]
	v_pk_mul_f32 v[94:95], v[118:119], v[94:95]
	v_pk_mul_f32 v[92:93], v[120:121], v[92:93]
	v_pk_mul_f32 v[90:91], v[122:123], v[90:91]
	v_pk_mul_f32 v[88:89], v[124:125], v[88:89]
	v_pk_mul_f32 v[86:87], v[126:127], v[86:87]
	v_pk_mul_f32 v[84:85], v[128:129], v[84:85]
	v_pk_mul_f32 v[82:83], v[156:157], v[82:83]
	v_cvt_f32_i32_e32 v66, v66
	v_cvt_f32_i32_e32 v69, v69
	v_cvt_f32_i32_e32 v68, v68
	v_pk_mul_f32 v[80:81], v[116:117], v[80:81]
	v_pk_mul_f32 v[78:79], v[118:119], v[78:79]
	v_pk_mul_f32 v[76:77], v[120:121], v[76:77]
	v_pk_mul_f32 v[74:75], v[122:123], v[74:75]
	v_pk_mul_f32 v[72:73], v[124:125], v[72:73]
	v_pk_mul_f32 v[70:71], v[126:127], v[70:71]
	v_pk_mul_f32 v[68:69], v[128:129], v[68:69]
	v_pk_mul_f32 v[66:67], v[156:157], v[66:67]
	v_cvt_f32_i32_e32 v55, v55
	v_cvt_f32_i32_e32 v54, v54
	v_cvt_f32_i32_e32 v57, v57
	v_cvt_f32_i32_e32 v56, v56
	v_cvt_f32_i32_e32 v51, v51
	v_cvt_f32_i32_e32 v50, v50
	v_cvt_f32_i32_e32 v53, v53
	v_cvt_f32_i32_e32 v52, v52
	v_cvt_f32_i32_e32 v63, v63
	v_cvt_f32_i32_e32 v62, v62
	v_cvt_f32_i32_e32 v65, v65
	v_cvt_f32_i32_e32 v64, v64
	v_cvt_f32_i32_e32 v59, v59
	v_cvt_f32_i32_e32 v58, v58
	v_cvt_f32_i32_e32 v61, v61
	v_cvt_f32_i32_e32 v60, v60
	v_pk_mul_f32 v[56:57], v[116:117], v[56:57]
	v_pk_mul_f32 v[54:55], v[118:119], v[54:55]
	v_pk_mul_f32 v[52:53], v[120:121], v[52:53]
	v_pk_mul_f32 v[50:51], v[122:123], v[50:51]
	v_pk_mul_f32 v[64:65], v[124:125], v[64:65]
	v_pk_mul_f32 v[62:63], v[126:127], v[62:63]
	v_pk_mul_f32 v[60:61], v[128:129], v[60:61]
	v_pk_mul_f32 v[58:59], v[156:157], v[58:59]
	v_cvt_f32_i32_e32 v39, v39
	v_cvt_f32_i32_e32 v38, v38
	v_cvt_f32_i32_e32 v41, v41
	v_cvt_f32_i32_e32 v40, v40
	v_cvt_f32_i32_e32 v35, v35
	v_cvt_f32_i32_e32 v34, v34
	v_cvt_f32_i32_e32 v37, v37
	v_cvt_f32_i32_e32 v36, v36
	v_cvt_f32_i32_e32 v47, v47
	v_cvt_f32_i32_e32 v46, v46
	v_cvt_f32_i32_e32 v49, v49
	v_cvt_f32_i32_e32 v48, v48
	v_cvt_f32_i32_e32 v43, v43
	v_cvt_f32_i32_e32 v42, v42
	v_cvt_f32_i32_e32 v45, v45
	v_cvt_f32_i32_e32 v44, v44
	v_pk_mul_f32 v[40:41], v[116:117], v[40:41]
	v_pk_mul_f32 v[38:39], v[118:119], v[38:39]
	v_pk_mul_f32 v[36:37], v[120:121], v[36:37]
	v_pk_mul_f32 v[34:35], v[122:123], v[34:35]
	v_pk_mul_f32 v[48:49], v[124:125], v[48:49]
	v_pk_mul_f32 v[46:47], v[126:127], v[46:47]
	s_nop 0
	v_pk_mul_f32 v[112:113], v[112:113], v[222:223] op_sel_hi:[1,0]
	v_pk_mul_f32 v[110:111], v[110:111], v[222:223] op_sel_hi:[1,0]
	v_pk_mul_f32 v[108:109], v[108:109], v[222:223] op_sel_hi:[1,0]
	v_pk_mul_f32 v[106:107], v[106:107], v[222:223] op_sel_hi:[1,0]
	v_pk_mul_f32 v[104:105], v[104:105], v[222:223] op_sel_hi:[1,0]
	v_pk_mul_f32 v[102:103], v[102:103], v[222:223] op_sel_hi:[1,0]
	v_pk_mul_f32 v[188:189], v[100:101], v[222:223] op_sel_hi:[1,0]
	v_pk_mul_f32 v[180:181], v[98:99], v[222:223] op_sel_hi:[1,0]
	v_cvt_pk_bf16_f32 v98, v110, v111
	v_cvt_pk_bf16_f32 v99, v112, v113
	v_cvt_pk_bf16_f32 v100, v106, v107
	v_cvt_pk_bf16_f32 v101, v108, v109
	v_cvt_pk_bf16_f32 v102, v102, v103
	v_cvt_pk_bf16_f32 v103, v104, v105
	v_cvt_pk_bf16_f32 v104, v180, v181
	v_cvt_pk_bf16_f32 v105, v188, v189
	global_store_dwordx4 v[184:185], v[98:101], off
	global_store_dwordx4 v[184:185], v[102:105], off offset:256
	s_nop 0
	v_or_b32_e32 v100, 48, v150
	v_mad_i64_i32 v[102:103], s[22:23], v182, s51, v[152:153]
	v_ashrrev_i32_e32 v101, 31, v100
	v_lshl_add_u64 v[102:103], v[102:103], 0, v[114:115]
	v_lshl_add_u64 v[104:105], v[100:101], 2, s[82:83]
	v_pk_mul_f32 v[44:45], v[128:129], v[44:45]
	v_pk_mul_f32 v[42:43], v[156:157], v[42:43]
	v_cvt_f32_i32_e32 v23, v23
	v_cvt_f32_i32_e32 v22, v22
	v_cvt_f32_i32_e32 v25, v25
	v_cvt_f32_i32_e32 v24, v24
	v_cvt_f32_i32_e32 v15, v15
	v_cvt_f32_i32_e32 v14, v14
	v_cvt_f32_i32_e32 v17, v17
	v_cvt_f32_i32_e32 v16, v16
	v_cvt_f32_i32_e32 v31, v31
	v_cvt_f32_i32_e32 v30, v30
	v_cvt_f32_i32_e32 v33, v33
	v_cvt_f32_i32_e32 v32, v32
	v_cvt_f32_i32_e32 v27, v27
	v_cvt_f32_i32_e32 v26, v26
	v_cvt_f32_i32_e32 v29, v29
	v_cvt_f32_i32_e32 v28, v28
	v_pk_mul_f32 v[24:25], v[116:117], v[24:25]
	v_pk_mul_f32 v[22:23], v[118:119], v[22:23]
	v_pk_mul_f32 v[16:17], v[120:121], v[16:17]
	v_pk_mul_f32 v[14:15], v[122:123], v[14:15]
	v_pk_mul_f32 v[32:33], v[124:125], v[32:33]
	v_pk_mul_f32 v[30:31], v[126:127], v[30:31]
	v_pk_mul_f32 v[28:29], v[128:129], v[28:29]
	v_pk_mul_f32 v[26:27], v[156:157], v[26:27]
	v_cvt_f32_i32_e32 v7, v7
	v_cvt_f32_i32_e32 v6, v6
	v_cvt_f32_i32_e32 v9, v9
	v_cvt_f32_i32_e32 v8, v8
	v_cvt_f32_i32_e32 v3, v3
	v_cvt_f32_i32_e32 v2, v2
	v_cvt_f32_i32_e32 v5, v5
	v_cvt_f32_i32_e32 v4, v4
	v_cvt_f32_i32_e32 v11, v11
	v_cvt_f32_i32_e32 v10, v10
	v_cvt_f32_i32_e32 v13, v13
	v_cvt_f32_i32_e32 v12, v12
	v_pk_mul_f32 v[8:9], v[116:117], v[8:9]
	v_pk_mul_f32 v[6:7], v[118:119], v[6:7]
	v_pk_mul_f32 v[4:5], v[120:121], v[4:5]
	v_pk_mul_f32 v[2:3], v[122:123], v[2:3]
	v_pk_mul_f32 v[12:13], v[128:129], v[12:13]
	v_pk_mul_f32 v[10:11], v[156:157], v[10:11]
	s_andn2_b64 vcc, exec, s[2:3]
	s_mov_b64 s[2:3], -1
	s_nop 0
	v_pk_mul_f32 v[96:97], v[96:97], v[224:225] op_sel_hi:[1,0]
	v_pk_mul_f32 v[94:95], v[94:95], v[224:225] op_sel_hi:[1,0]
	v_pk_mul_f32 v[92:93], v[92:93], v[224:225] op_sel_hi:[1,0]
	v_pk_mul_f32 v[90:91], v[90:91], v[224:225] op_sel_hi:[1,0]
	v_pk_mul_f32 v[88:89], v[88:89], v[224:225] op_sel_hi:[1,0]
	v_pk_mul_f32 v[86:87], v[86:87], v[224:225] op_sel_hi:[1,0]
	v_pk_mul_f32 v[106:107], v[84:85], v[224:225] op_sel_hi:[1,0]
	v_pk_mul_f32 v[98:99], v[82:83], v[224:225] op_sel_hi:[1,0]
	v_cvt_pk_bf16_f32 v82, v94, v95
	v_cvt_pk_bf16_f32 v83, v96, v97
	v_cvt_pk_bf16_f32 v84, v90, v91
	v_cvt_pk_bf16_f32 v85, v92, v93
	v_cvt_pk_bf16_f32 v86, v86, v87
	v_cvt_pk_bf16_f32 v87, v88, v89
	v_cvt_pk_bf16_f32 v88, v98, v99
	v_cvt_pk_bf16_f32 v89, v106, v107
	global_store_dwordx4 v[102:103], v[82:85], off
	global_store_dwordx4 v[102:103], v[86:89], off offset:256
	s_nop 0
	v_mad_i64_i32 v[84:85], s[22:23], v100, s51, v[152:153]
	v_lshl_add_u64 v[84:85], v[84:85], 0, v[114:115]
	s_nop 0
	v_pk_mul_f32 v[80:81], v[80:81], v[226:227] op_sel_hi:[1,0]
	v_pk_mul_f32 v[78:79], v[78:79], v[226:227] op_sel_hi:[1,0]
	v_pk_mul_f32 v[76:77], v[76:77], v[226:227] op_sel_hi:[1,0]
	v_pk_mul_f32 v[74:75], v[74:75], v[226:227] op_sel_hi:[1,0]
	v_pk_mul_f32 v[72:73], v[72:73], v[226:227] op_sel_hi:[1,0]
	v_pk_mul_f32 v[70:71], v[70:71], v[226:227] op_sel_hi:[1,0]
	v_pk_mul_f32 v[86:87], v[68:69], v[226:227] op_sel_hi:[1,0]
	v_pk_mul_f32 v[82:83], v[66:67], v[226:227] op_sel_hi:[1,0]
	v_cvt_pk_bf16_f32 v66, v78, v79
	v_cvt_pk_bf16_f32 v67, v80, v81
	v_cvt_pk_bf16_f32 v68, v74, v75
	v_cvt_pk_bf16_f32 v69, v76, v77
	v_cvt_pk_bf16_f32 v70, v70, v71
	v_cvt_pk_bf16_f32 v71, v72, v73
	v_cvt_pk_bf16_f32 v72, v82, v83
	v_cvt_pk_bf16_f32 v73, v86, v87
	global_store_dwordx4 v[84:85], v[66:69], off
	global_store_dwordx4 v[84:85], v[70:73], off offset:256
	s_nop 0
	v_add_u32_e32 v67, 0x80, v150
	v_mad_i64_i32 v[68:69], s[22:23], v67, s51, v[152:153]
	v_lshl_add_u64 v[68:69], v[68:69], 0, v[114:115]
	s_nop 0
	v_pk_mul_f32 v[56:57], v[56:57], v[228:229] op_sel_hi:[1,0]
	v_pk_mul_f32 v[54:55], v[54:55], v[228:229] op_sel_hi:[1,0]
	v_pk_mul_f32 v[70:71], v[52:53], v[228:229] op_sel_hi:[1,0]
	v_pk_mul_f32 v[52:53], v[50:51], v[228:229] op_sel_hi:[1,0]
	v_pk_mul_f32 v[64:65], v[64:65], v[228:229] op_sel_hi:[1,0]
	v_pk_mul_f32 v[62:63], v[62:63], v[228:229] op_sel_hi:[1,0]
	v_pk_mul_f32 v[60:61], v[60:61], v[228:229] op_sel_hi:[1,0]
	v_pk_mul_f32 v[58:59], v[58:59], v[228:229] op_sel_hi:[1,0]
	v_cvt_pk_bf16_f32 v50, v54, v55
	v_cvt_pk_bf16_f32 v51, v56, v57
	v_cvt_pk_bf16_f32 v52, v52, v53
	v_cvt_pk_bf16_f32 v53, v70, v71
	v_cvt_pk_bf16_f32 v54, v62, v63
	v_cvt_pk_bf16_f32 v55, v64, v65
	v_cvt_pk_bf16_f32 v56, v58, v59
	v_cvt_pk_bf16_f32 v57, v60, v61
	global_store_dwordx4 v[68:69], v[50:53], off
	global_store_dwordx4 v[68:69], v[54:57], off offset:256
	s_nop 0
	v_add_u32_e32 v51, 0x90, v150
	v_mad_i64_i32 v[52:53], s[22:23], v51, s51, v[152:153]
	v_lshl_add_u64 v[52:53], v[52:53], 0, v[114:115]
	s_nop 0
	v_pk_mul_f32 v[40:41], v[40:41], v[230:231] op_sel_hi:[1,0]
	v_pk_mul_f32 v[38:39], v[38:39], v[230:231] op_sel_hi:[1,0]
	v_pk_mul_f32 v[54:55], v[36:37], v[230:231] op_sel_hi:[1,0]
	v_pk_mul_f32 v[36:37], v[34:35], v[230:231] op_sel_hi:[1,0]
	v_pk_mul_f32 v[48:49], v[48:49], v[230:231] op_sel_hi:[1,0]
	v_pk_mul_f32 v[46:47], v[46:47], v[230:231] op_sel_hi:[1,0]
	v_pk_mul_f32 v[44:45], v[44:45], v[230:231] op_sel_hi:[1,0]
	v_pk_mul_f32 v[42:43], v[42:43], v[230:231] op_sel_hi:[1,0]
	v_cvt_pk_bf16_f32 v34, v38, v39
	v_cvt_pk_bf16_f32 v35, v40, v41
	v_cvt_pk_bf16_f32 v36, v36, v37
	v_cvt_pk_bf16_f32 v37, v54, v55
	v_cvt_pk_bf16_f32 v38, v46, v47
	v_cvt_pk_bf16_f32 v39, v48, v49
	v_cvt_pk_bf16_f32 v40, v42, v43
	v_cvt_pk_bf16_f32 v41, v44, v45
	global_store_dwordx4 v[52:53], v[34:37], off
	global_store_dwordx4 v[52:53], v[38:41], off offset:256
	s_nop 0
	v_add_u32_e32 v35, 0xa0, v150
	v_mad_i64_i32 v[36:37], s[22:23], v35, s51, v[152:153]
	v_lshl_add_u64 v[36:37], v[36:37], 0, v[114:115]
	s_nop 0
	v_pk_mul_f32 v[24:25], v[24:25], v[232:233] op_sel_hi:[1,0]
	v_pk_mul_f32 v[22:23], v[22:23], v[232:233] op_sel_hi:[1,0]
	v_pk_mul_f32 v[38:39], v[16:17], v[232:233] op_sel_hi:[1,0]
	v_pk_mul_f32 v[16:17], v[14:15], v[232:233] op_sel_hi:[1,0]
	v_pk_mul_f32 v[32:33], v[32:33], v[232:233] op_sel_hi:[1,0]
	v_pk_mul_f32 v[30:31], v[30:31], v[232:233] op_sel_hi:[1,0]
	v_pk_mul_f32 v[28:29], v[28:29], v[232:233] op_sel_hi:[1,0]
	v_pk_mul_f32 v[26:27], v[26:27], v[232:233] op_sel_hi:[1,0]
	v_cvt_pk_bf16_f32 v14, v22, v23
	v_cvt_pk_bf16_f32 v15, v24, v25
	v_cvt_pk_bf16_f32 v16, v16, v17
	v_cvt_pk_bf16_f32 v17, v38, v39
	v_cvt_pk_bf16_f32 v22, v30, v31
	v_cvt_pk_bf16_f32 v23, v32, v33
	v_cvt_pk_bf16_f32 v24, v26, v27
	v_cvt_pk_bf16_f32 v25, v28, v29
	global_store_dwordx4 v[36:37], v[14:17], off
	global_store_dwordx4 v[36:37], v[22:25], off offset:256
	s_nop 0
	v_cvt_f32_i32_e32 v17, v19
	v_cvt_f32_i32_e32 v16, v18
	v_cvt_f32_i32_e32 v19, v21
	v_cvt_f32_i32_e32 v18, v20
	v_add_u32_e32 v15, 0xb0, v150
	v_mad_i64_i32 v[20:21], s[22:23], v15, s51, v[152:153]
	v_pk_mul_f32 v[18:19], v[124:125], v[18:19]
	v_pk_mul_f32 v[16:17], v[126:127], v[16:17]
	v_lshl_add_u64 v[20:21], v[20:21], 0, v[114:115]
	s_nop 0
	v_pk_mul_f32 v[8:9], v[8:9], v[234:235] op_sel_hi:[1,0]
	v_pk_mul_f32 v[6:7], v[6:7], v[234:235] op_sel_hi:[1,0]
	v_pk_mul_f32 v[22:23], v[4:5], v[234:235] op_sel_hi:[1,0]
	v_pk_mul_f32 v[4:5], v[2:3], v[234:235] op_sel_hi:[1,0]
	v_pk_mul_f32 v[18:19], v[18:19], v[234:235] op_sel_hi:[1,0]
	v_pk_mul_f32 v[16:17], v[16:17], v[234:235] op_sel_hi:[1,0]
	v_pk_mul_f32 v[12:13], v[12:13], v[234:235] op_sel_hi:[1,0]
	v_pk_mul_f32 v[10:11], v[10:11], v[234:235] op_sel_hi:[1,0]
	v_cvt_pk_bf16_f32 v2, v6, v7
	v_cvt_pk_bf16_f32 v3, v8, v9
	v_cvt_pk_bf16_f32 v4, v4, v5
	v_cvt_pk_bf16_f32 v5, v22, v23
	v_cvt_pk_bf16_f32 v6, v16, v17
	v_cvt_pk_bf16_f32 v7, v18, v19
	v_cvt_pk_bf16_f32 v8, v10, v11
	v_cvt_pk_bf16_f32 v9, v12, v13
	global_store_dwordx4 v[20:21], v[2:5], off
	global_store_dwordx4 v[20:21], v[6:9], off offset:256
	s_cbranch_vccnz .LBB0_193
	s_andn2_b64 vcc, exec, s[0:1]
	s_cbranch_vccnz .LBB0_192
	s_barrier
	s_branch .LBB0_192
